# top-n loop: wave maximum by two row_bcast DPP steps and one readlane per token (was four readlanes and three s_max)
# baseline (speedup 1.0000x reference)
; #define PL_SWAP16(a, b) asm("s_nop 1\n\tv_permlane16_swap_b32 %0, %1" : "+v"(a), "+v"(b))
; #define PL_SWAP32(a, b) asm("s_nop 1\n\tv_permlane32_swap_b32 %0, %1" : "+v"(a), "+v"(b))
; #define DPP_U(v, ctrl) ((unsigned)__builtin_amdgcn_mov_dpp((int)(v), (ctrl), 0xF, 0xF, true))
; #define CE_(i, j) do { const unsigned hi_ = umax_(k[i], k[j]), lo_ = umin_(k[i], k[j]); k[i] = hi_; k[j] = lo_; } while (0)
; __device__ __forceinline__ unsigned wave_max_u(unsigned v) {
;     v = umax_(v, DPP_U(v, 0xB1)); v = umax_(v, DPP_U(v, 0x4E)); v = umax_(v, DPP_U(v, 0x141)); v = umax_(v, DPP_U(v, 0x140));
;     { unsigned a = v, b = v; PL_SWAP16(a, b); v = umax_(a, b); } { unsigned a = v, b = v; PL_SWAP32(a, b); v = umax_(a, b); }
;     return v;
; }
; __device__ __forceinline__ void sort4_desc(unsigned (&k)[4]) {
;     ...
;     CE_(0, 1); CE_(2, 3); CE_(0, 2); CE_(1, 3); CE_(1, 2);
;     ...
; }
; __device__ __forceinline__ void topn_round_u(unsigned (&k)[4], unsigned& pm, int lane) {
;     const unsigned wm = wave_max_u(k[0]);
;     const unsigned long long bal = __ballot(k[0] == wm); const int L = __ffsll((long long)bal) - 1;
;     const bool isL = lane == L;
;     pm |= isL ? (8u >> (k[0] & 3u)) : 0u;
;     k[0] = isL ? k[1] : k[0]; k[1] = isL ? k[2] : k[1]; k[2] = isL ? k[3] : k[2]; k[3] = isL ? 0u : k[3];
; }
; __device__ __forceinline__ void cmp_phase(Frame& F) {
;     ...
;                 for (int r = 0; r < TOPN - 3; ++r) { topn_round_u(ka, pa, lane); topn_round_u(kb2, pb, lane); topn_round_u(kc, pc, lane); topn_round_u(kd, pd, lane); }
;                 const unsigned bt = 1u << tk;
; #pragma unroll
;                 for (int q = 0; q < 4; ++q) pick[q] |= (((pa >> q) & 1u) ? bt : 0u) | (((pb >> q) & 1u) ? (bt << 1) : 0u) | (((pc >> q) & 1u) ? (bt << 2) : 0u) | (((pd >> q) & 1u) ? (bt << 3) : 0u);
.LBB0_1622:
	v_max_u32_dpp v24, v6, v6 quad_perm:[1,0,3,2] row_mask:0xf bank_mask:0xf bound_ctrl:1
	v_max_u32_dpp v26, v12, v12 quad_perm:[1,0,3,2] row_mask:0xf bank_mask:0xf bound_ctrl:1
	v_max_u32_dpp v28, v16, v16 quad_perm:[1,0,3,2] row_mask:0xf bank_mask:0xf bound_ctrl:1
	v_max_u32_dpp v30, v20, v20 quad_perm:[1,0,3,2] row_mask:0xf bank_mask:0xf bound_ctrl:1
	v_max_u32_dpp v24, v24, v24 quad_perm:[2,3,0,1] row_mask:0xf bank_mask:0xf bound_ctrl:1
	v_max_u32_dpp v26, v26, v26 quad_perm:[2,3,0,1] row_mask:0xf bank_mask:0xf bound_ctrl:1
	v_max_u32_dpp v28, v28, v28 quad_perm:[2,3,0,1] row_mask:0xf bank_mask:0xf bound_ctrl:1
	v_max_u32_dpp v30, v30, v30 quad_perm:[2,3,0,1] row_mask:0xf bank_mask:0xf bound_ctrl:1
	v_max_u32_dpp v24, v24, v24 row_half_mirror row_mask:0xf bank_mask:0xf bound_ctrl:1
	v_max_u32_dpp v26, v26, v26 row_half_mirror row_mask:0xf bank_mask:0xf bound_ctrl:1
	v_max_u32_dpp v28, v28, v28 row_half_mirror row_mask:0xf bank_mask:0xf bound_ctrl:1
	v_max_u32_dpp v30, v30, v30 row_half_mirror row_mask:0xf bank_mask:0xf bound_ctrl:1
	v_max_u32_dpp v24, v24, v24 row_mirror row_mask:0xf bank_mask:0xf bound_ctrl:1
	v_max_u32_dpp v26, v26, v26 row_mirror row_mask:0xf bank_mask:0xf bound_ctrl:1
	v_max_u32_dpp v28, v28, v28 row_mirror row_mask:0xf bank_mask:0xf bound_ctrl:1
	v_max_u32_dpp v30, v30, v30 row_mirror row_mask:0xf bank_mask:0xf bound_ctrl:1
	v_max_u32_dpp v24, v24, v24 row_bcast:15 row_mask:0xa bank_mask:0xf
	v_max_u32_dpp v26, v26, v26 row_bcast:15 row_mask:0xa bank_mask:0xf
	v_max_u32_dpp v28, v28, v28 row_bcast:15 row_mask:0xa bank_mask:0xf
	v_max_u32_dpp v30, v30, v30 row_bcast:15 row_mask:0xa bank_mask:0xf
	v_max_u32_dpp v24, v24, v24 row_bcast:31 row_mask:0xc bank_mask:0xf
	v_max_u32_dpp v26, v26, v26 row_bcast:31 row_mask:0xc bank_mask:0xf
	v_max_u32_dpp v28, v28, v28 row_bcast:31 row_mask:0xc bank_mask:0xf
	v_max_u32_dpp v30, v30, v30 row_bcast:31 row_mask:0xc bank_mask:0xf
	v_readlane_b32 s18, v24, 63
	v_readlane_b32 s24, v26, 63
	v_readlane_b32 s48, v28, 63
	v_readlane_b32 s74, v30, 63
	v_cmp_eq_u32_e32 vcc, s18, v6
	s_ff1_i32_b64 s76, vcc
	s_lshl_b64 s[100:101], 1, s76
	v_cndmask_b32_e64 v6, v6, v9, s[100:101]
	v_cndmask_b32_e64 v9, v9, v11, s[100:101]
	v_cndmask_b32_e64 v11, v11, v8, s[100:101]
	v_cndmask_b32_e64 v8, v8, 0, s[100:101]
	v_addc_co_u32_e64 v243, s[98:99], 0, v243, s[100:101]
	v_cmp_eq_u32_e32 vcc, s24, v12
	s_ff1_i32_b64 s76, vcc
	s_lshl_b64 s[100:101], 1, s76
	v_cndmask_b32_e64 v12, v12, v14, s[100:101]
	v_cndmask_b32_e64 v14, v14, v15, s[100:101]
	v_cndmask_b32_e64 v15, v15, v13, s[100:101]
	v_cndmask_b32_e64 v13, v13, 0, s[100:101]
	v_addc_co_u32_e64 v244, s[98:99], 0, v244, s[100:101]
	v_cmp_eq_u32_e32 vcc, s48, v16
	s_ff1_i32_b64 s76, vcc
	s_lshl_b64 s[100:101], 1, s76
	v_cndmask_b32_e64 v16, v16, v18, s[100:101]
	v_cndmask_b32_e64 v18, v18, v19, s[100:101]
	v_cndmask_b32_e64 v19, v19, v17, s[100:101]
	v_cndmask_b32_e64 v17, v17, 0, s[100:101]
	v_addc_co_u32_e64 v245, s[98:99], 0, v245, s[100:101]
	v_cmp_eq_u32_e32 vcc, s74, v20
	s_ff1_i32_b64 s76, vcc
	s_lshl_b64 s[100:101], 1, s76
	v_cndmask_b32_e64 v20, v20, v22, s[100:101]
	v_cndmask_b32_e64 v22, v22, v23, s[100:101]
	v_cndmask_b32_e64 v23, v23, v21, s[100:101]
	v_cndmask_b32_e64 v21, v21, 0, s[100:101]
	v_addc_co_u32_e64 v246, s[98:99], 0, v246, s[100:101]
	s_add_i32 s37, s37, -1
	s_cmp_eq_u32 s37, 0
	s_cbranch_scc0 .LBB0_1622
	v_lshlrev_b32_e32 v24, 2, v243
	v_bfe_u32 v24, v239, 0, v24
	v_lshrrev_b32_e32 v25, 8, v24
	v_or_b32_e32 v24, v24, v25
	v_lshrrev_b32_e32 v25, 4, v24
	v_or_b32_e32 v24, v24, v25
	v_and_b32_e32 v10, 15, v24
	v_lshlrev_b32_e32 v24, 2, v244
	v_bfe_u32 v24, v240, 0, v24
	v_lshrrev_b32_e32 v25, 8, v24
	v_or_b32_e32 v24, v24, v25
	v_lshrrev_b32_e32 v25, 4, v24
	v_or_b32_e32 v24, v24, v25
	v_and_b32_e32 v7, 15, v24
	v_lshlrev_b32_e32 v24, 2, v245
	v_bfe_u32 v24, v241, 0, v24
	v_lshrrev_b32_e32 v25, 8, v24
	v_or_b32_e32 v24, v24, v25
	v_lshrrev_b32_e32 v25, 4, v24
	v_or_b32_e32 v24, v24, v25
	v_and_b32_e32 v5, 15, v24
	v_lshlrev_b32_e32 v24, 2, v246
	v_bfe_u32 v24, v242, 0, v24
	v_lshrrev_b32_e32 v25, 8, v24
	v_or_b32_e32 v24, v24, v25
	v_lshrrev_b32_e32 v25, 4, v24
	v_or_b32_e32 v24, v24, v25
	v_and_b32_e32 v4, 15, v24
	s_lshl_b32 s18, 1, s36
	s_lshl_b32 s19, 2, s36
	v_bfe_i32 v6, v10, 0, 1
	v_bfe_i32 v8, v7, 0, 1
	v_and_b32_e32 v6, s18, v6
	v_and_b32_e32 v8, s19, v8
	v_or3_b32 v3, v6, v3, v8
	v_bfe_i32 v6, v10, 1, 1
	v_bfe_i32 v8, v7, 1, 1
	s_lshl_b32 s22, 4, s36
	s_lshl_b32 s23, 8, s36
	v_bfe_i32 v9, v5, 0, 1
	v_bfe_i32 v11, v4, 0, 1
	v_and_b32_e32 v6, s18, v6
	v_and_b32_e32 v8, s19, v8
	v_and_b32_e32 v9, s22, v9
	v_and_b32_e32 v11, s23, v11
	v_or3_b32 v2, v6, v2, v8
	v_bfe_i32 v6, v10, 2, 1
	v_bfe_i32 v8, v7, 2, 1
	v_or3_b32 v3, v3, v9, v11
	v_bfe_i32 v9, v5, 1, 1
	v_bfe_i32 v11, v4, 1, 1
	v_and_b32_e32 v6, s18, v6
	v_and_b32_e32 v8, s19, v8
	v_and_b32_e32 v9, s22, v9
	v_and_b32_e32 v11, s23, v11
	v_or3_b32 v1, v6, v1, v8
	v_bfe_i32 v6, v10, 3, 1
	v_bfe_i32 v7, v7, 3, 1
	v_or3_b32 v2, v2, v9, v11
	v_bfe_i32 v9, v5, 2, 1
	v_bfe_i32 v11, v4, 2, 1
	v_and_b32_e32 v6, s18, v6
	v_and_b32_e32 v7, s19, v7
	v_bfe_i32 v5, v5, 3, 1
	v_bfe_i32 v4, v4, 3, 1
	v_and_b32_e32 v9, s22, v9
	v_and_b32_e32 v11, s23, v11
	v_and_b32_e32 v5, s22, v5
	v_and_b32_e32 v4, s23, v4
	v_or3_b32 v0, v6, v0, v7
	v_or3_b32 v1, v1, v9, v11
	v_or3_b32 v0, v0, v5, v4
	s_mov_b64 s[18:19], 0
	s_and_b64 vcc, exec, s[60:61]
	s_cbranch_vccnz .LBB0_1625
	s_mov_b32 s36, 4
	s_branch .LBB0_1605
